# speedup vs baseline: 1.0109x; 1.0109x over previous
.LBB1_117:
	s_andn2_b64 vcc, exec, s[20:21]
	s_cbranch_vccnz .LBB1_126
	s_waitcnt lgkmcnt(0)
	s_load_dwordx4 s[8:11], s[0:1], 0x0
	s_bfe_u32 s4, s2, 0x20005
	s_lshl_b32 s0, s2, 6
	v_and_b32_e32 v10, 63, v0
	s_and_b32 s3, s0, 0x7c0
	s_mul_i32 s7, s4, 0x6000
	s_waitcnt lgkmcnt(0)
	s_add_u32 s0, s8, s7
	v_or_b32_e32 v1, s3, v10
	s_addc_u32 s1, s9, 0
	v_lshlrev_b32_e32 v2, 2, v1
	v_mov_b32_e32 v3, 0
	v_lshl_add_u64 v[4:5], s[0:1], 0, v[2:3]
	s_movk_i32 s5, 0x2000
	v_add_co_u32_e32 v6, vcc, s5, v4
	s_movk_i32 s5, 0x4000
	s_nop 0
	v_addc_co_u32_e32 v7, vcc, 0, v5, vcc
	v_add_co_u32_e32 v4, vcc, s5, v4
	v_readfirstlane_b32 s5, v0
	s_nop 0
	v_addc_co_u32_e32 v5, vcc, 0, v5, vcc
	global_load_dword v11, v2, s[0:1]
	global_load_dword v12, v[6:7], off
	global_load_dword v13, v[4:5], off
	s_lshr_b32 s6, s5, 6
	s_cmpk_lt_u32 s2, 0x80
	s_cselect_b32 s8, s8, s10
	s_cselect_b32 s0, s9, s11
	s_add_u32 s7, s8, s7
	s_mov_b32 s1, 0
	s_addc_u32 s8, s0, 0
	s_lshl_b32 s0, s6, 8
	s_lshl_b64 s[0:1], s[0:1], 2
	s_add_u32 s7, s7, s0
	s_addc_u32 s8, s8, s1
	v_mov_b32_e32 v9, 0x7f800000
	s_mov_b64 s[0:1], 0
	v_mov_b32_e32 v14, 0x2000
	v_mov_b32_e32 v15, 0x4000
	v_mov_b32_e32 v8, 0x7f800000
	v_mov_b32_e32 v7, 0x7f800000
	v_mov_b32_e32 v6, 0x7f800000
	v_mov_b32_e32 v5, 0x7f800000
	v_mov_b32_e32 v4, 0x7f800000
	v_mov_b32_e32 v2, 0x7f800000
	v_mov_b32_e32 v1, 0x7f800000
	s_mov_b32 s10, s7
	s_mov_b32 s11, s8
	s_load_dwordx8 s[20:27], s[10:11], 0x0
	s_load_dwordx8 s[28:35], s[10:11], 0x2000
	s_load_dwordx8 s[36:43], s[10:11], 0x4000
	s_mov_b32 s0, 0
	s_waitcnt vmcnt(0) lgkmcnt(0)
.Lknn_loop:
	s_add_u32 s10, s7, s0
	s_addc_u32 s11, s8, 0
	s_load_dwordx8 s[44:51], s[10:11], 0x20
	s_load_dwordx8 s[52:59], s[10:11], 0x2020
	s_load_dwordx8 s[60:67], s[10:11], 0x4020
	v_subrev_f32_e32 v16, s20, v11
	v_subrev_f32_e32 v24, s28, v12
	v_subrev_f32_e32 v32, s36, v13
	v_mul_f32_e32 v16, v16, v16
	v_fmac_f32_e32 v16, v24, v24
	v_fmac_f32_e32 v16, v32, v32
	v_subrev_f32_e32 v17, s21, v11
	v_subrev_f32_e32 v25, s29, v12
	v_subrev_f32_e32 v33, s37, v13
	v_mul_f32_e32 v17, v17, v17
	v_fmac_f32_e32 v17, v25, v25
	v_fmac_f32_e32 v17, v33, v33
	v_subrev_f32_e32 v18, s22, v11
	v_subrev_f32_e32 v26, s30, v12
	v_subrev_f32_e32 v34, s38, v13
	v_mul_f32_e32 v18, v18, v18
	v_fmac_f32_e32 v18, v26, v26
	v_fmac_f32_e32 v18, v34, v34
	v_med3_f32 v1, v16, v2, v1
	v_med3_f32 v2, v16, v4, v2
	v_med3_f32 v4, v16, v5, v4
	v_med3_f32 v5, v16, v6, v5
	v_med3_f32 v6, v16, v7, v6
	v_med3_f32 v7, v16, v8, v7
	v_med3_f32 v8, v16, v9, v8
	v_min_f32_e32 v9, v9, v16
	v_subrev_f32_e32 v19, s23, v11
	v_subrev_f32_e32 v27, s31, v12
	v_subrev_f32_e32 v35, s39, v13
	v_mul_f32_e32 v19, v19, v19
	v_fmac_f32_e32 v19, v27, v27
	v_fmac_f32_e32 v19, v35, v35
	v_med3_f32 v1, v17, v2, v1
	v_med3_f32 v2, v17, v4, v2
	v_med3_f32 v4, v17, v5, v4
	v_med3_f32 v5, v17, v6, v5
	v_med3_f32 v6, v17, v7, v6
	v_med3_f32 v7, v17, v8, v7
	v_med3_f32 v8, v17, v9, v8
	v_min_f32_e32 v9, v9, v17
	v_subrev_f32_e32 v20, s24, v11
	v_subrev_f32_e32 v28, s32, v12
	v_subrev_f32_e32 v36, s40, v13
	v_mul_f32_e32 v20, v20, v20
	v_fmac_f32_e32 v20, v28, v28
	v_fmac_f32_e32 v20, v36, v36
	v_med3_f32 v1, v18, v2, v1
	v_med3_f32 v2, v18, v4, v2
	v_med3_f32 v4, v18, v5, v4
	v_med3_f32 v5, v18, v6, v5
	v_med3_f32 v6, v18, v7, v6
	v_med3_f32 v7, v18, v8, v7
	v_med3_f32 v8, v18, v9, v8
	v_min_f32_e32 v9, v9, v18
	v_subrev_f32_e32 v21, s25, v11
	v_subrev_f32_e32 v29, s33, v12
	v_subrev_f32_e32 v37, s41, v13
	v_mul_f32_e32 v21, v21, v21
	v_fmac_f32_e32 v21, v29, v29
	v_fmac_f32_e32 v21, v37, v37
	v_med3_f32 v1, v19, v2, v1
	v_med3_f32 v2, v19, v4, v2
	v_med3_f32 v4, v19, v5, v4
	v_med3_f32 v5, v19, v6, v5
	v_med3_f32 v6, v19, v7, v6
	v_med3_f32 v7, v19, v8, v7
	v_med3_f32 v8, v19, v9, v8
	v_min_f32_e32 v9, v9, v19
	v_subrev_f32_e32 v22, s26, v11
	v_subrev_f32_e32 v30, s34, v12
	v_subrev_f32_e32 v38, s42, v13
	v_mul_f32_e32 v22, v22, v22
	v_fmac_f32_e32 v22, v30, v30
	v_fmac_f32_e32 v22, v38, v38
	v_med3_f32 v1, v20, v2, v1
	v_med3_f32 v2, v20, v4, v2
	v_med3_f32 v4, v20, v5, v4
	v_med3_f32 v5, v20, v6, v5
	v_med3_f32 v6, v20, v7, v6
	v_med3_f32 v7, v20, v8, v7
	v_med3_f32 v8, v20, v9, v8
	v_min_f32_e32 v9, v9, v20
	v_subrev_f32_e32 v23, s27, v11
	v_subrev_f32_e32 v31, s35, v12
	v_subrev_f32_e32 v39, s43, v13
	v_mul_f32_e32 v23, v23, v23
	v_fmac_f32_e32 v23, v31, v31
	v_fmac_f32_e32 v23, v39, v39
	v_med3_f32 v1, v21, v2, v1
	v_med3_f32 v2, v21, v4, v2
	v_med3_f32 v4, v21, v5, v4
	v_med3_f32 v5, v21, v6, v5
	v_med3_f32 v6, v21, v7, v6
	v_med3_f32 v7, v21, v8, v7
	v_med3_f32 v8, v21, v9, v8
	v_min_f32_e32 v9, v9, v21
	v_med3_f32 v1, v22, v2, v1
	v_med3_f32 v2, v22, v4, v2
	v_med3_f32 v4, v22, v5, v4
	v_med3_f32 v5, v22, v6, v5
	v_med3_f32 v6, v22, v7, v6
	v_med3_f32 v7, v22, v8, v7
	v_med3_f32 v8, v22, v9, v8
	v_min_f32_e32 v9, v9, v22
	v_med3_f32 v1, v23, v2, v1
	v_med3_f32 v2, v23, v4, v2
	v_med3_f32 v4, v23, v5, v4
	v_med3_f32 v5, v23, v6, v5
	v_med3_f32 v6, v23, v7, v6
	v_med3_f32 v7, v23, v8, v7
	v_med3_f32 v8, v23, v9, v8
	v_min_f32_e32 v9, v9, v23
	s_add_u32 s12, s0, 64
	s_min_u32 s12, s12, 0x3e0
	s_add_u32 s10, s7, s12
	s_addc_u32 s11, s8, 0
	s_waitcnt lgkmcnt(0)
	s_load_dwordx8 s[20:27], s[10:11], 0x0
	s_load_dwordx8 s[28:35], s[10:11], 0x2000
	s_load_dwordx8 s[36:43], s[10:11], 0x4000
	v_subrev_f32_e32 v16, s44, v11
	v_subrev_f32_e32 v24, s52, v12
	v_subrev_f32_e32 v32, s60, v13
	v_mul_f32_e32 v16, v16, v16
	v_fmac_f32_e32 v16, v24, v24
	v_fmac_f32_e32 v16, v32, v32
	v_subrev_f32_e32 v17, s45, v11
	v_subrev_f32_e32 v25, s53, v12
	v_subrev_f32_e32 v33, s61, v13
	v_mul_f32_e32 v17, v17, v17
	v_fmac_f32_e32 v17, v25, v25
	v_fmac_f32_e32 v17, v33, v33
	v_subrev_f32_e32 v18, s46, v11
	v_subrev_f32_e32 v26, s54, v12
	v_subrev_f32_e32 v34, s62, v13
	v_mul_f32_e32 v18, v18, v18
	v_fmac_f32_e32 v18, v26, v26
	v_fmac_f32_e32 v18, v34, v34
	v_med3_f32 v1, v16, v2, v1
	v_med3_f32 v2, v16, v4, v2
	v_med3_f32 v4, v16, v5, v4
	v_med3_f32 v5, v16, v6, v5
	v_med3_f32 v6, v16, v7, v6
	v_med3_f32 v7, v16, v8, v7
	v_med3_f32 v8, v16, v9, v8
	v_min_f32_e32 v9, v9, v16
	v_subrev_f32_e32 v19, s47, v11
	v_subrev_f32_e32 v27, s55, v12
	v_subrev_f32_e32 v35, s63, v13
	v_mul_f32_e32 v19, v19, v19
	v_fmac_f32_e32 v19, v27, v27
	v_fmac_f32_e32 v19, v35, v35
	v_med3_f32 v1, v17, v2, v1
	v_med3_f32 v2, v17, v4, v2
	v_med3_f32 v4, v17, v5, v4
	v_med3_f32 v5, v17, v6, v5
	v_med3_f32 v6, v17, v7, v6
	v_med3_f32 v7, v17, v8, v7
	v_med3_f32 v8, v17, v9, v8
	v_min_f32_e32 v9, v9, v17
	v_subrev_f32_e32 v20, s48, v11
	v_subrev_f32_e32 v28, s56, v12
	v_subrev_f32_e32 v36, s64, v13
	v_mul_f32_e32 v20, v20, v20
	v_fmac_f32_e32 v20, v28, v28
	v_fmac_f32_e32 v20, v36, v36
	v_med3_f32 v1, v18, v2, v1
	v_med3_f32 v2, v18, v4, v2
	v_med3_f32 v4, v18, v5, v4
	v_med3_f32 v5, v18, v6, v5
	v_med3_f32 v6, v18, v7, v6
	v_med3_f32 v7, v18, v8, v7
	v_med3_f32 v8, v18, v9, v8
	v_min_f32_e32 v9, v9, v18
	v_subrev_f32_e32 v21, s49, v11
	v_subrev_f32_e32 v29, s57, v12
	v_subrev_f32_e32 v37, s65, v13
	v_mul_f32_e32 v21, v21, v21
	v_fmac_f32_e32 v21, v29, v29
	v_fmac_f32_e32 v21, v37, v37
	v_med3_f32 v1, v19, v2, v1
	v_med3_f32 v2, v19, v4, v2
	v_med3_f32 v4, v19, v5, v4
	v_med3_f32 v5, v19, v6, v5
	v_med3_f32 v6, v19, v7, v6
	v_med3_f32 v7, v19, v8, v7
	v_med3_f32 v8, v19, v9, v8
	v_min_f32_e32 v9, v9, v19
	v_subrev_f32_e32 v22, s50, v11
	v_subrev_f32_e32 v30, s58, v12
	v_subrev_f32_e32 v38, s66, v13
	v_mul_f32_e32 v22, v22, v22
	v_fmac_f32_e32 v22, v30, v30
	v_fmac_f32_e32 v22, v38, v38
	v_med3_f32 v1, v20, v2, v1
	v_med3_f32 v2, v20, v4, v2
	v_med3_f32 v4, v20, v5, v4
	v_med3_f32 v5, v20, v6, v5
	v_med3_f32 v6, v20, v7, v6
	v_med3_f32 v7, v20, v8, v7
	v_med3_f32 v8, v20, v9, v8
	v_min_f32_e32 v9, v9, v20
	v_subrev_f32_e32 v23, s51, v11
	v_subrev_f32_e32 v31, s59, v12
	v_subrev_f32_e32 v39, s67, v13
	v_mul_f32_e32 v23, v23, v23
	v_fmac_f32_e32 v23, v31, v31
	v_fmac_f32_e32 v23, v39, v39
	v_med3_f32 v1, v21, v2, v1
	v_med3_f32 v2, v21, v4, v2
	v_med3_f32 v4, v21, v5, v4
	v_med3_f32 v5, v21, v6, v5
	v_med3_f32 v6, v21, v7, v6
	v_med3_f32 v7, v21, v8, v7
	v_med3_f32 v8, v21, v9, v8
	v_min_f32_e32 v9, v9, v21
	v_med3_f32 v1, v22, v2, v1
	v_med3_f32 v2, v22, v4, v2
	v_med3_f32 v4, v22, v5, v4
	v_med3_f32 v5, v22, v6, v5
	v_med3_f32 v6, v22, v7, v6
	v_med3_f32 v7, v22, v8, v7
	v_med3_f32 v8, v22, v9, v8
	v_min_f32_e32 v9, v9, v22
	v_med3_f32 v1, v23, v2, v1
	v_med3_f32 v2, v23, v4, v2
	v_med3_f32 v4, v23, v5, v4
	v_med3_f32 v5, v23, v6, v5
	v_med3_f32 v6, v23, v7, v6
	v_med3_f32 v7, v23, v8, v7
	v_med3_f32 v8, v23, v9, v8
	v_min_f32_e32 v9, v9, v23
	s_add_u32 s0, s0, 64
	s_cmpk_eq_i32 s0, 0x400
	s_waitcnt lgkmcnt(0)
	s_cbranch_scc0 .Lknn_loop
	v_lshlrev_b32_e32 v3, 2, v10
	v_lshl_or_b32 v10, s6, 11, v3
	s_cmpk_lt_u32 s5, 0x100
	ds_write2st64_b32 v10, v9, v8 offset1:1
	ds_write2st64_b32 v10, v7, v6 offset0:2 offset1:3
	ds_write2st64_b32 v10, v5, v4 offset0:4 offset1:5
	ds_write2st64_b32 v10, v2, v1 offset0:6 offset1:7
	s_waitcnt lgkmcnt(0)
	s_barrier
	s_cbranch_scc0 .LBB1_122
	ds_read2st64_b32 v[12:13], v10 offset0:32 offset1:33
	ds_read2st64_b32 v[14:15], v10 offset0:34 offset1:35
	ds_read2st64_b32 v[16:17], v10 offset0:36 offset1:37
	ds_read2st64_b32 v[18:19], v10 offset0:38 offset1:39
	v_max_f32_e32 v11, v9, v9
	s_waitcnt lgkmcnt(2)
	v_max_f32_e32 v21, v14, v14
	v_max_f32_e32 v20, v12, v12
	v_min_f32_e32 v11, v11, v20
	v_max_f32_e32 v20, v13, v13
	v_med3_f32 v9, v12, v9, v8
	v_med3_f32 v8, v12, v8, v7
	v_med3_f32 v7, v12, v7, v6
	v_med3_f32 v6, v12, v6, v5
	v_med3_f32 v5, v12, v5, v4
	v_med3_f32 v4, v12, v4, v2
	v_min_f32_e32 v20, v11, v20
	v_med3_f32 v11, v13, v11, v9
	v_med3_f32 v9, v13, v9, v8
	v_med3_f32 v8, v13, v8, v7
	v_med3_f32 v7, v13, v7, v6
	v_med3_f32 v6, v13, v6, v5
	v_med3_f32 v5, v13, v5, v4
	v_med3_f32 v1, v12, v2, v1
	v_min_f32_e32 v21, v20, v21
	v_max_f32_e32 v22, v15, v15
	v_med3_f32 v20, v14, v20, v11
	v_med3_f32 v11, v14, v11, v9
	v_med3_f32 v9, v14, v9, v8
	v_med3_f32 v8, v14, v8, v7
	v_med3_f32 v7, v14, v7, v6
	v_med3_f32 v6, v14, v6, v5
	v_med3_f32 v1, v13, v4, v1
	v_min_f32_e32 v22, v21, v22
	s_waitcnt lgkmcnt(1)
	v_max_f32_e32 v23, v16, v16
	v_med3_f32 v21, v15, v21, v20
	v_med3_f32 v20, v15, v20, v11
	v_med3_f32 v11, v15, v11, v9
	v_med3_f32 v9, v15, v9, v8
	v_med3_f32 v8, v15, v8, v7
	v_med3_f32 v7, v15, v7, v6
	v_med3_f32 v1, v14, v5, v1
	v_min_f32_e32 v23, v22, v23
	v_max_f32_e32 v24, v17, v17
	v_med3_f32 v22, v16, v22, v21
	v_med3_f32 v21, v16, v21, v20
	v_med3_f32 v20, v16, v20, v11
	v_med3_f32 v11, v16, v11, v9
	v_med3_f32 v9, v16, v9, v8
	v_med3_f32 v8, v16, v8, v7
	v_med3_f32 v1, v15, v6, v1
	v_min_f32_e32 v24, v23, v24
	s_waitcnt lgkmcnt(0)
	v_max_f32_e32 v25, v18, v18
	v_med3_f32 v23, v17, v23, v22
	v_med3_f32 v22, v17, v22, v21
	v_med3_f32 v21, v17, v21, v20
	v_med3_f32 v20, v17, v20, v11
	v_med3_f32 v11, v17, v11, v9
	v_med3_f32 v9, v17, v9, v8
	v_med3_f32 v1, v16, v7, v1
	v_min_f32_e32 v25, v24, v25
	v_max_f32_e32 v26, v19, v19
	v_med3_f32 v24, v18, v24, v23
	v_med3_f32 v23, v18, v23, v22
	v_med3_f32 v22, v18, v22, v21
	v_med3_f32 v21, v18, v21, v20
	v_med3_f32 v20, v18, v20, v11
	v_med3_f32 v11, v18, v11, v9
	v_med3_f32 v1, v17, v8, v1
	v_min_f32_e32 v26, v25, v26
	v_med3_f32 v25, v19, v25, v24
	v_med3_f32 v24, v19, v24, v23
	v_med3_f32 v23, v19, v23, v22
	v_med3_f32 v22, v19, v22, v21
	v_med3_f32 v21, v19, v21, v20
	v_med3_f32 v20, v19, v20, v11
	v_med3_f32 v1, v18, v9, v1
	v_med3_f32 v1, v19, v11, v1
	v_mov_b32_e32 v9, v26
	v_mov_b32_e32 v8, v25
	v_mov_b32_e32 v7, v24
	v_mov_b32_e32 v6, v23
	v_mov_b32_e32 v5, v22
	v_mov_b32_e32 v4, v21
	v_mov_b32_e32 v2, v20
	ds_write2st64_b32 v10, v26, v25 offset1:1
	ds_write2st64_b32 v10, v24, v23 offset0:2 offset1:3
	ds_write2st64_b32 v10, v22, v21 offset0:4 offset1:5
	ds_write2st64_b32 v10, v20, v1 offset0:6 offset1:7

.LBB3_393:
	s_endpgm
	s_nop 0
	s_nop 0
	s_nop 0
	s_nop 0
	s_nop 0
	s_nop 0
	s_nop 0
	s_nop 0
	s_nop 0
	s_nop 0
	s_nop 0
	s_nop 0
	s_nop 0
	s_nop 0
	s_nop 0
	s_nop 0

.LBB4_21:
	s_add_i32 s1, s8, s0
	s_add_i32 s6, s1, -4
	s_min_u32 s1, s6, s1
	s_mul_i32 s6, s1, 0xc0
	v_add_u32_e32 v139, s6, v138
	ds_read_b128 v[140:143], v139
	ds_read_b128 v[146:149], v139 offset:64
	ds_read_b128 v[150:153], v139 offset:12544
	ds_read_b128 v[154:157], v139 offset:128
	ds_read_b128 v[158:161], v139 offset:12608
	ds_read_b128 v[162:165], v139 offset:12672
	s_mul_i32 s6, s1, 0x600
	s_addk_i32 s6, 0x600
	s_cmp_lt_i32 s1, 3
	s_cselect_b32 s6, s6, 0
	s_ashr_i32 s7, s6, 31
	s_setprio 1
	s_waitcnt vmcnt(17) lgkmcnt(5)
	v_mfma_f32_16x16x32_bf16 v[118:121], v[140:143], v[74:77], v[118:121]
	s_waitcnt lgkmcnt(3)
	v_mfma_f32_16x16x32_bf16 v[114:117], v[150:153], v[74:77], v[114:117]
	s_waitcnt vmcnt(16)
	v_mfma_f32_16x16x32_bf16 v[110:113], v[140:143], v[62:65], v[110:113]
	v_mfma_f32_16x16x32_bf16 v[106:109], v[150:153], v[62:65], v[106:109]
	s_waitcnt vmcnt(15)
	v_mfma_f32_16x16x32_bf16 v[102:105], v[140:143], v[66:69], v[102:105]
	v_mfma_f32_16x16x32_bf16 v[98:101], v[150:153], v[66:69], v[98:101]
	s_waitcnt vmcnt(14)
	v_mfma_f32_16x16x32_bf16 v[94:97], v[140:143], v[58:61], v[94:97]
	v_mfma_f32_16x16x32_bf16 v[90:93], v[150:153], v[58:61], v[90:93]
	s_waitcnt vmcnt(13)
	v_mfma_f32_16x16x32_bf16 v[86:89], v[140:143], v[70:73], v[86:89]
	v_mfma_f32_16x16x32_bf16 v[82:85], v[150:153], v[70:73], v[82:85]
	s_waitcnt vmcnt(12)
	v_mfma_f32_16x16x32_bf16 v[78:81], v[140:143], v[54:57], v[78:81]
	v_mfma_f32_16x16x32_bf16 v[6:9], v[150:153], v[54:57], v[6:9]
	s_setprio 0
	s_lshl_b64 s[6:7], s[6:7], 1
	v_lshl_add_u64 v[140:141], v[122:123], 0, s[6:7]
	v_lshl_add_u64 v[150:151], v[126:127], 0, s[6:7]
	v_lshl_add_u64 v[166:167], v[130:131], 0, s[6:7]
	v_lshl_add_u64 v[142:143], v[124:125], 0, s[6:7]
	global_load_dwordx4 v[74:77], v[140:141], off
	global_load_dwordx4 v[62:65], v[142:143], off
	v_lshl_add_u64 v[152:153], v[128:129], 0, s[6:7]
	global_load_dwordx4 v[66:69], v[150:151], off
	global_load_dwordx4 v[58:61], v[152:153], off
	v_lshl_add_u64 v[168:169], v[132:133], 0, s[6:7]
	global_load_dwordx4 v[70:73], v[166:167], off
	global_load_dwordx4 v[54:57], v[168:169], off
	s_setprio 1
	s_waitcnt vmcnt(17)
	v_mfma_f32_16x16x32_bf16 v[118:121], v[146:149], v[50:53], v[118:121]
	s_waitcnt lgkmcnt(1)
	v_mfma_f32_16x16x32_bf16 v[114:117], v[158:161], v[50:53], v[114:117]
	s_waitcnt vmcnt(16)
	v_mfma_f32_16x16x32_bf16 v[110:113], v[146:149], v[38:41], v[110:113]
	v_mfma_f32_16x16x32_bf16 v[106:109], v[158:161], v[38:41], v[106:109]
	s_waitcnt vmcnt(15)
	v_mfma_f32_16x16x32_bf16 v[102:105], v[146:149], v[46:49], v[102:105]
	v_mfma_f32_16x16x32_bf16 v[98:101], v[158:161], v[46:49], v[98:101]
	s_waitcnt vmcnt(14)
	v_mfma_f32_16x16x32_bf16 v[94:97], v[146:149], v[34:37], v[94:97]
	v_mfma_f32_16x16x32_bf16 v[90:93], v[158:161], v[34:37], v[90:93]
	s_waitcnt vmcnt(13)
	v_mfma_f32_16x16x32_bf16 v[86:89], v[146:149], v[42:45], v[86:89]
	v_mfma_f32_16x16x32_bf16 v[82:85], v[158:161], v[42:45], v[82:85]
	s_waitcnt vmcnt(12)
	v_mfma_f32_16x16x32_bf16 v[78:81], v[146:149], v[10:13], v[78:81]
	v_mfma_f32_16x16x32_bf16 v[6:9], v[158:161], v[10:13], v[6:9]
	s_setprio 0
	global_load_dwordx4 v[50:53], v[140:141], off offset:1024
	global_load_dwordx4 v[38:41], v[142:143], off offset:1024
	global_load_dwordx4 v[46:49], v[150:151], off offset:1024
	global_load_dwordx4 v[34:37], v[152:153], off offset:1024
	global_load_dwordx4 v[42:45], v[166:167], off offset:1024
	global_load_dwordx4 v[10:13], v[168:169], off offset:1024
	s_setprio 1
	s_waitcnt vmcnt(17)
	v_mfma_f32_16x16x32_bf16 v[118:121], v[154:157], v[26:29], v[118:121]
	s_waitcnt lgkmcnt(0)
	v_mfma_f32_16x16x32_bf16 v[114:117], v[162:165], v[26:29], v[114:117]
	s_waitcnt vmcnt(16)
	v_mfma_f32_16x16x32_bf16 v[110:113], v[154:157], v[30:33], v[110:113]
	v_mfma_f32_16x16x32_bf16 v[106:109], v[162:165], v[30:33], v[106:109]
	s_waitcnt vmcnt(15)
	v_mfma_f32_16x16x32_bf16 v[102:105], v[154:157], v[22:25], v[102:105]
	v_mfma_f32_16x16x32_bf16 v[98:101], v[162:165], v[22:25], v[98:101]
	s_waitcnt vmcnt(14)
	v_mfma_f32_16x16x32_bf16 v[94:97], v[154:157], v[18:21], v[94:97]
	v_mfma_f32_16x16x32_bf16 v[90:93], v[162:165], v[18:21], v[90:93]
	s_waitcnt vmcnt(13)
	v_mfma_f32_16x16x32_bf16 v[86:89], v[154:157], v[14:17], v[86:89]
	v_mfma_f32_16x16x32_bf16 v[82:85], v[162:165], v[14:17], v[82:85]
	s_waitcnt vmcnt(12)
	v_mfma_f32_16x16x32_bf16 v[78:81], v[154:157], v[2:5], v[78:81]
	v_mfma_f32_16x16x32_bf16 v[6:9], v[162:165], v[2:5], v[6:9]
	s_setprio 0
	global_load_dwordx4 v[26:29], v[140:141], off offset:2048
	global_load_dwordx4 v[30:33], v[142:143], off offset:2048
	global_load_dwordx4 v[22:25], v[150:151], off offset:2048
	global_load_dwordx4 v[18:21], v[152:153], off offset:2048
	global_load_dwordx4 v[14:17], v[166:167], off offset:2048
	global_load_dwordx4 v[2:5], v[168:169], off offset:2048
	s_add_i32 s0, s0, 1
	s_cmp_lg_u32 s0, 3
	s_cbranch_scc1 .LBB4_21
	s_mul_i32 s0, s8, 0x60
	s_add_i32 s6, s0, 0xffffffa0
	s_and_b64 s[0:1], s[2:3], exec
	s_cselect_b32 s0, 0x120, s6
	v_lshl_add_u32 v137, s0, 1, v137
	ds_read_b128 v[122:125], v137 offset:50176
	ds_read_b128 v[126:129], v137 offset:50240
	ds_read_b128 v[130:133], v137 offset:62720
	ds_read_b128 v[138:141], v137 offset:50304
	ds_read_b128 v[146:149], v137 offset:62784
	ds_read_b128 v[150:153], v137 offset:62848
	s_setprio 1
	s_waitcnt vmcnt(17) lgkmcnt(5)
	v_mfma_f32_16x16x32_bf16 v[118:121], v[122:125], v[74:77], v[118:121]
	s_waitcnt lgkmcnt(3)
	v_mfma_f32_16x16x32_bf16 v[74:77], v[130:133], v[74:77], v[114:117]
	s_waitcnt vmcnt(16)
	v_mfma_f32_16x16x32_bf16 v[110:113], v[122:125], v[62:65], v[110:113]
	v_mfma_f32_16x16x32_bf16 v[62:65], v[130:133], v[62:65], v[106:109]
	s_waitcnt vmcnt(15)
	v_mfma_f32_16x16x32_bf16 v[102:105], v[122:125], v[66:69], v[102:105]
	v_mfma_f32_16x16x32_bf16 v[66:69], v[130:133], v[66:69], v[98:101]
	s_waitcnt vmcnt(14)
	v_mfma_f32_16x16x32_bf16 v[94:97], v[122:125], v[58:61], v[94:97]
	v_mfma_f32_16x16x32_bf16 v[58:61], v[130:133], v[58:61], v[90:93]
	s_waitcnt vmcnt(13)
	v_mfma_f32_16x16x32_bf16 v[86:89], v[122:125], v[70:73], v[86:89]
	v_mfma_f32_16x16x32_bf16 v[70:73], v[130:133], v[70:73], v[82:85]
	s_waitcnt vmcnt(12)
	v_mfma_f32_16x16x32_bf16 v[78:81], v[122:125], v[54:57], v[78:81]
	v_mfma_f32_16x16x32_bf16 v[6:9], v[130:133], v[54:57], v[6:9]
	s_setprio 0
	s_setprio 1
	s_waitcnt vmcnt(11)
	v_mfma_f32_16x16x32_bf16 v[54:57], v[126:129], v[50:53], v[118:121]
	s_waitcnt lgkmcnt(1)
	v_mfma_f32_16x16x32_bf16 v[50:53], v[146:149], v[50:53], v[74:77]
	s_waitcnt vmcnt(10)
	v_mfma_f32_16x16x32_bf16 v[74:77], v[126:129], v[38:41], v[110:113]
	v_mfma_f32_16x16x32_bf16 v[38:41], v[146:149], v[38:41], v[62:65]
	s_waitcnt vmcnt(9)
	v_mfma_f32_16x16x32_bf16 v[62:65], v[126:129], v[46:49], v[102:105]
	v_mfma_f32_16x16x32_bf16 v[66:69], v[146:149], v[46:49], v[66:69]
	s_waitcnt vmcnt(8)
	v_mfma_f32_16x16x32_bf16 v[82:85], v[126:129], v[34:37], v[94:97]
	v_mfma_f32_16x16x32_bf16 v[58:61], v[146:149], v[34:37], v[58:61]
	s_waitcnt vmcnt(7)
	v_mfma_f32_16x16x32_bf16 v[86:89], v[126:129], v[42:45], v[86:89]
	v_mfma_f32_16x16x32_bf16 v[70:73], v[146:149], v[42:45], v[70:73]
	s_waitcnt vmcnt(6)
	v_mfma_f32_16x16x32_bf16 v[78:81], v[126:129], v[10:13], v[78:81]
	v_mfma_f32_16x16x32_bf16 v[90:93], v[146:149], v[10:13], v[6:9]
	s_setprio 0
	s_setprio 1
	s_waitcnt vmcnt(5)
	v_mfma_f32_16x16x32_bf16 v[54:57], v[138:141], v[26:29], v[54:57]
	s_waitcnt lgkmcnt(0)
	v_mfma_f32_16x16x32_bf16 v[46:49], v[150:153], v[26:29], v[50:53]
	s_waitcnt vmcnt(4)
	v_mfma_f32_16x16x32_bf16 v[42:45], v[138:141], v[30:33], v[74:77]
	v_mfma_f32_16x16x32_bf16 v[38:41], v[150:153], v[30:33], v[38:41]
	s_waitcnt vmcnt(3)
	v_mfma_f32_16x16x32_bf16 v[34:37], v[138:141], v[22:25], v[62:65]
	v_mfma_f32_16x16x32_bf16 v[30:33], v[150:153], v[22:25], v[66:69]
	s_waitcnt vmcnt(2)
	v_mfma_f32_16x16x32_bf16 v[26:29], v[138:141], v[18:21], v[82:85]
	v_mfma_f32_16x16x32_bf16 v[22:25], v[150:153], v[18:21], v[58:61]
	s_waitcnt vmcnt(1)
	v_mfma_f32_16x16x32_bf16 v[18:21], v[138:141], v[14:17], v[86:89]
	v_mfma_f32_16x16x32_bf16 v[10:13], v[150:153], v[14:17], v[70:73]
	s_waitcnt vmcnt(0)
	v_mfma_f32_16x16x32_bf16 v[6:9], v[138:141], v[2:5], v[78:81]
	v_mfma_f32_16x16x32_bf16 v[2:5], v[150:153], v[2:5], v[90:93]
	s_setprio 0
	v_or_b32_e32 v14, v145, v136
	v_lshlrev_b32_e32 v15, 2, v14
	global_load_dword v16, v15, s[26:27]
	global_load_dword v17, v15, s[26:27] offset:64
	v_add_u32_e32 v60, v145, v136
	v_lshlrev_b32_e32 v62, 2, v60
	global_load_dword v63, v62, s[26:27] offset:128
	global_load_dword v71, v62, s[26:27] offset:192
	global_load_dword v72, v62, s[26:27] offset:256
	global_load_dword v73, v62, s[26:27] offset:320
	s_movk_i32 s1, 0x100
	v_mov_b32_e32 v15, 0x3e38aa3b
	v_cmp_gt_u32_e32 vcc, s1, v0
	s_movk_i32 s0, 0x610
	v_mov_b32_e32 v50, 0xc20
	v_cndmask_b32_e32 v15, 1.0, v15, vcc
	v_mov_b32_e32 v51, 0x1230
	v_mov_b32_e32 v52, 0x6100
	v_mov_b32_e32 v53, 0x6710
	v_mov_b32_e32 v58, 0x6d20
	v_mov_b32_e32 v59, 0x7330
	v_lshlrev_b32_e32 v14, 1, v14
	v_mad_u32_u24 v61, v135, s0, s0
	v_mad_u32_u24 v50, v135, s0, v50
	v_mad_u32_u24 v51, v135, s0, v51
	v_mad_u32_u24 v52, v135, s0, v52
	v_mad_u32_u24 v53, v135, s0, v53
	v_mad_u32_u24 v58, v135, s0, v58
	v_mad_u32_u24 v59, v135, s0, v59
	v_mad_u32_u24 v64, v135, s0, v14
	v_add_u32_e32 v65, v14, v61
	v_add_u32_e32 v66, v14, v50
	v_add_u32_e32 v67, v14, v51
	v_add_u32_e32 v68, v14, v52
	v_add_u32_e32 v69, v14, v53
	v_add_u32_e32 v70, v14, v58
	v_add_u32_e32 v14, v14, v59
	s_movk_i32 s1, 0x2ab
	s_movk_i32 s6, 0x600
	s_waitcnt vmcnt(5)
	v_add_f32_e32 v54, v16, v54
	v_add_f32_e32 v55, v16, v55
	v_add_f32_e32 v56, v16, v56
	v_add_f32_e32 v57, v16, v57
	v_add_f32_e32 v46, v16, v46
	v_add_f32_e32 v47, v16, v47
	v_add_f32_e32 v48, v16, v48
	v_add_f32_e32 v16, v16, v49
	s_waitcnt vmcnt(4)
	v_add_f32_e32 v42, v17, v42
	v_add_f32_e32 v43, v17, v43
	v_add_f32_e32 v44, v17, v44
	v_add_f32_e32 v45, v17, v45
	v_mul_f32_e32 v49, v15, v54
	v_mul_f32_e32 v16, v15, v16
	v_add_f32_e32 v38, v17, v38
	v_mul_f32_e32 v54, v15, v55
	v_mul_f32_e32 v55, v15, v56
	v_mul_f32_e32 v56, v15, v57
	v_mul_f32_e32 v46, v15, v46
	v_mul_f32_e32 v47, v15, v47
	v_mul_f32_e32 v48, v15, v48
	v_mul_f32_e32 v42, v15, v42
	v_mul_f32_e32 v43, v15, v43
	v_mul_f32_e32 v44, v15, v44
	v_mul_f32_e32 v45, v15, v45
	v_cvt_pk_bf16_f32 v49, v49, s0
	v_cvt_pk_bf16_f32 v16, v16, s0
	v_cvt_pk_bf16_f32 v54, v54, s0
	v_cvt_pk_bf16_f32 v55, v55, s0
	v_cvt_pk_bf16_f32 v56, v56, s0
	v_cvt_pk_bf16_f32 v46, v46, s0
	v_cvt_pk_bf16_f32 v47, v47, s0
	v_cvt_pk_bf16_f32 v48, v48, s0
	v_cvt_pk_bf16_f32 v42, v42, s0
	v_cvt_pk_bf16_f32 v43, v43, s0
	v_cvt_pk_bf16_f32 v44, v44, s0
	v_cvt_pk_bf16_f32 v45, v45, s0
	ds_write_b16 v64, v49
	ds_write_b16 v65, v54
	ds_write_b16 v66, v55
	ds_write_b16 v67, v56
	ds_write_b16 v68, v46
	ds_write_b16 v69, v47
	ds_write_b16 v70, v48
	ds_write_b16 v14, v16
	ds_write_b16 v64, v42 offset:32
	ds_write_b16 v65, v43 offset:32
	ds_write_b16 v66, v44 offset:32
	ds_write_b16 v67, v45 offset:32
	v_mul_f32_e32 v16, v15, v38
	v_cvt_pk_bf16_f32 v16, v16, s0
	ds_write_b16 v68, v16 offset:32
	v_add_f32_e32 v16, v17, v39
	v_mul_f32_e32 v16, v15, v16
	v_cvt_pk_bf16_f32 v16, v16, s0
	ds_write_b16 v69, v16 offset:32
	v_add_f32_e32 v16, v17, v40
	v_mul_f32_e32 v16, v15, v16
	v_cvt_pk_bf16_f32 v16, v16, s0
	ds_write_b16 v70, v16 offset:32
	v_add_f32_e32 v16, v17, v41
	v_mul_f32_e32 v16, v15, v16
	v_cvt_pk_bf16_f32 v16, v16, s0
	ds_write_b16 v14, v16 offset:32
	s_waitcnt vmcnt(3)
	v_add_f32_e32 v16, v63, v34
	v_lshlrev_b32_e32 v14, 1, v60
	v_mul_f32_e32 v16, v15, v16
	v_cvt_pk_bf16_f32 v16, v16, s0
	v_mad_u32_u24 v17, v135, s0, v14
	ds_write_b16 v17, v16 offset:64
	v_add_f32_e32 v16, v63, v35
	v_mul_f32_e32 v16, v15, v16
	v_cvt_pk_bf16_f32 v16, v16, s0
	v_add_u32_e32 v34, v14, v61
	ds_write_b16 v34, v16 offset:64
	v_add_f32_e32 v16, v63, v36
	v_mul_f32_e32 v16, v15, v16
	v_cvt_pk_bf16_f32 v16, v16, s0
	v_add_u32_e32 v35, v14, v50
	ds_write_b16 v35, v16 offset:64
	v_add_f32_e32 v16, v63, v37
	v_mul_f32_e32 v16, v15, v16
	v_cvt_pk_bf16_f32 v16, v16, s0
	v_add_u32_e32 v36, v14, v51
	ds_write_b16 v36, v16 offset:64
	v_add_f32_e32 v16, v63, v30
	v_mul_f32_e32 v16, v15, v16
	v_cvt_pk_bf16_f32 v16, v16, s0
	v_add_u32_e32 v30, v14, v52
	ds_write_b16 v30, v16 offset:64
	v_add_f32_e32 v16, v63, v31
	v_mul_f32_e32 v16, v15, v16
	v_cvt_pk_bf16_f32 v16, v16, s0
	v_add_u32_e32 v31, v14, v53
	ds_write_b16 v31, v16 offset:64
	v_add_f32_e32 v16, v63, v32
	v_mul_f32_e32 v16, v15, v16
	v_cvt_pk_bf16_f32 v16, v16, s0
	v_add_u32_e32 v32, v14, v58
	ds_write_b16 v32, v16 offset:64
	v_add_f32_e32 v16, v63, v33
	v_mul_f32_e32 v16, v15, v16
	v_cvt_pk_bf16_f32 v16, v16, s0
	v_add_u32_e32 v14, v14, v59
	ds_write_b16 v14, v16 offset:64
	s_waitcnt vmcnt(2)
	v_add_f32_e32 v16, v71, v26
	v_mul_f32_e32 v16, v15, v16
	v_cvt_pk_bf16_f32 v16, v16, s0
	ds_write_b16 v17, v16 offset:96
	v_add_f32_e32 v16, v71, v27
	v_mul_f32_e32 v16, v15, v16
	v_cvt_pk_bf16_f32 v16, v16, s0
	ds_write_b16 v34, v16 offset:96
	v_add_f32_e32 v16, v71, v28
	v_mul_f32_e32 v16, v15, v16
	v_cvt_pk_bf16_f32 v16, v16, s0
	ds_write_b16 v35, v16 offset:96
	v_add_f32_e32 v16, v71, v29
	v_mul_f32_e32 v16, v15, v16
	v_cvt_pk_bf16_f32 v16, v16, s0
	ds_write_b16 v36, v16 offset:96
	v_add_f32_e32 v16, v71, v22
	v_mul_f32_e32 v16, v15, v16
	v_cvt_pk_bf16_f32 v16, v16, s0
	ds_write_b16 v30, v16 offset:96
	v_add_f32_e32 v16, v71, v23
	v_mul_f32_e32 v16, v15, v16
	v_cvt_pk_bf16_f32 v16, v16, s0
	ds_write_b16 v31, v16 offset:96
	v_add_f32_e32 v16, v71, v24
	v_mul_f32_e32 v16, v15, v16
	v_cvt_pk_bf16_f32 v16, v16, s0
	ds_write_b16 v32, v16 offset:96
	v_add_f32_e32 v16, v71, v25
	v_mul_f32_e32 v16, v15, v16
	v_cvt_pk_bf16_f32 v16, v16, s0
	ds_write_b16 v14, v16 offset:96
	s_waitcnt vmcnt(1)
	v_add_f32_e32 v16, v72, v18
	v_add_f32_e32 v10, v72, v10
	v_mul_f32_e32 v16, v15, v16
	v_mul_f32_e32 v10, v15, v10
	v_cvt_pk_bf16_f32 v16, v16, s0
	v_cvt_pk_bf16_f32 v10, v10, s0
	ds_write_b16 v17, v16 offset:128
	v_add_f32_e32 v16, v72, v19
	ds_write_b16 v30, v10 offset:128
	v_add_f32_e32 v10, v72, v11
	v_mul_f32_e32 v16, v15, v16
	v_mul_f32_e32 v10, v15, v10
	v_cvt_pk_bf16_f32 v16, v16, s0
	v_cvt_pk_bf16_f32 v10, v10, s0
	ds_write_b16 v34, v16 offset:128
	v_add_f32_e32 v16, v72, v20
	ds_write_b16 v31, v10 offset:128
	v_add_f32_e32 v10, v72, v12
	v_mul_f32_e32 v16, v15, v16
	v_mul_f32_e32 v10, v15, v10
	v_cvt_pk_bf16_f32 v16, v16, s0
	v_cvt_pk_bf16_f32 v10, v10, s0
	ds_write_b16 v35, v16 offset:128
	v_add_f32_e32 v16, v72, v21
	ds_write_b16 v32, v10 offset:128
	v_add_f32_e32 v10, v72, v13
	s_waitcnt vmcnt(0)
	v_add_f32_e32 v6, v73, v6
	v_add_f32_e32 v2, v73, v2
	v_mul_f32_e32 v16, v15, v16
	v_mul_f32_e32 v10, v15, v10
	v_mul_f32_e32 v6, v15, v6
	v_mul_f32_e32 v2, v15, v2
	v_cvt_pk_bf16_f32 v16, v16, s0
	v_cvt_pk_bf16_f32 v10, v10, s0
	v_cvt_pk_bf16_f32 v6, v6, s0
	v_cvt_pk_bf16_f32 v2, v2, s0
	ds_write_b16 v36, v16 offset:128
	ds_write_b16 v14, v10 offset:128
	ds_write_b16 v17, v6 offset:160
	v_add_f32_e32 v6, v73, v7
	ds_write_b16 v30, v2 offset:160
	v_add_f32_e32 v2, v73, v3
	v_mul_f32_e32 v6, v15, v6
	v_mul_f32_e32 v2, v15, v2
	v_cvt_pk_bf16_f32 v6, v6, s0
	v_cvt_pk_bf16_f32 v2, v2, s0
	ds_write_b16 v34, v6 offset:160
	v_add_f32_e32 v6, v73, v8
	ds_write_b16 v31, v2 offset:160
	v_add_f32_e32 v2, v73, v4
	v_mul_f32_e32 v6, v15, v6
	v_mul_f32_e32 v2, v15, v2
	v_cvt_pk_bf16_f32 v6, v6, s0
	v_cvt_pk_bf16_f32 v2, v2, s0
	ds_write_b16 v35, v6 offset:160
	v_add_f32_e32 v6, v73, v9
	ds_write_b16 v32, v2 offset:160
	v_add_f32_e32 v2, v73, v5
	v_mul_f32_e32 v6, v15, v6
	v_mul_f32_e32 v2, v15, v2
	v_cvt_pk_bf16_f32 v6, v6, s0
	v_cvt_pk_bf16_f32 v2, v2, s0
	ds_write_b16 v36, v6 offset:160
	ds_write_b16 v14, v2 offset:160
	v_mul_u32_u24_sdwa v2, v0, s1 dst_sel:DWORD dst_unused:UNUSED_PAD src0_sel:WORD_0 src1_sel:DWORD
	v_lshrrev_b32_e32 v6, 16, v2
	v_mul_lo_u16_e32 v2, 0x60, v6
	v_sub_u16_e32 v2, v0, v2
	v_lshlrev_b16_e32 v2, 3, v2
	v_lshlrev_b32_e32 v10, 1, v2
	v_mad_u32_u24 v2, v6, s0, v10
	v_or_b32_e32 v6, s28, v6
	v_mov_b64_e32 v[12:13], s[4:5]
	v_mad_i64_i32 v[6:7], s[2:3], v6, s6, v[12:13]
	v_mov_b32_e32 v11, 0
	v_lshl_add_u64 v[14:15], v[6:7], 0, v[10:11]
	v_mul_u32_u24_sdwa v6, v1, s1 dst_sel:DWORD dst_unused:UNUSED_PAD src0_sel:WORD_0 src1_sel:DWORD
	v_lshrrev_b32_e32 v16, 16, v6
	v_mul_lo_u16_e32 v6, 0x60, v16
	v_sub_u16_e32 v1, v1, v6
	v_lshlrev_b16_e32 v1, 3, v1
	s_waitcnt lgkmcnt(0)
	s_barrier
	ds_read_b128 v[2:5], v2
	v_lshlrev_b32_e32 v10, 1, v1
	v_mad_u32_u24 v1, v16, s0, v10
	ds_read_b128 v[6:9], v1
	v_or_b32_e32 v1, s28, v16
	s_waitcnt lgkmcnt(1)
	global_store_dwordx4 v[14:15], v[2:5], off
	s_nop 1
	v_mad_i64_i32 v[2:3], s[2:3], v1, s6, v[12:13]
	v_mul_u32_u24_sdwa v1, v134, s1 dst_sel:DWORD dst_unused:UNUSED_PAD src0_sel:WORD_0 src1_sel:DWORD
	v_lshl_add_u64 v[2:3], v[2:3], 0, v[10:11]
	v_lshrrev_b32_e32 v1, 16, v1
	s_waitcnt lgkmcnt(0)
	global_store_dwordx4 v[2:3], v[6:9], off
	v_mul_lo_u16_e32 v2, 0x60, v1
	v_sub_u16_e32 v2, v134, v2
	v_lshlrev_b16_e32 v2, 3, v2
	v_lshlrev_b32_e32 v10, 1, v2
	v_mad_u32_u24 v2, v1, s0, v10
	v_or_b32_e32 v1, s28, v1
	v_mad_i64_i32 v[6:7], s[2:3], v1, s6, v[12:13]
	v_or_b32_e32 v1, 0x600, v0
	v_lshl_add_u64 v[14:15], v[6:7], 0, v[10:11]
	v_mul_u32_u24_e32 v6, 0x2ab, v1
	v_lshrrev_b32_e32 v16, 16, v6
	v_mul_lo_u16_e32 v6, 0x60, v16
	v_sub_u16_e32 v1, v1, v6
	v_lshlrev_b16_e32 v1, 3, v1
	ds_read_b128 v[2:5], v2
	v_lshlrev_b32_e32 v10, 1, v1
	v_mad_u32_u24 v1, v16, s0, v10
	ds_read_b128 v[6:9], v1
	v_add_u32_e32 v1, s28, v16
	s_waitcnt lgkmcnt(1)
	global_store_dwordx4 v[14:15], v[2:5], off
	s_nop 1
	v_mad_i64_i32 v[2:3], s[2:3], v1, s6, v[12:13]
	v_lshl_add_u64 v[2:3], v[2:3], 0, v[10:11]
	v_or_b32_e32 v1, 0x800, v0
	s_waitcnt lgkmcnt(0)
	global_store_dwordx4 v[2:3], v[6:9], off
	v_mul_u32_u24_e32 v2, 0xaab, v1
	v_or_b32_e32 v0, 0xa00, v0
	v_lshrrev_b32_e32 v6, 18, v2
	v_mul_lo_u16_e32 v2, 0x60, v6
	v_sub_u16_e32 v1, v1, v2
	v_lshlrev_b16_e32 v1, 3, v1
	v_lshlrev_b32_e32 v10, 1, v1
	v_mad_u32_u24 v1, v6, s0, v10
	ds_read_b128 v[2:5], v1
	v_or_b32_e32 v1, s28, v6
	v_mad_i64_i32 v[6:7], s[2:3], v1, s6, v[12:13]
	v_mul_u32_u24_e32 v1, 0xaab, v0
	v_lshrrev_b32_e32 v1, 18, v1
	v_lshl_add_u64 v[14:15], v[6:7], 0, v[10:11]
	v_mul_lo_u16_e32 v6, 0x60, v1
	v_sub_u16_e32 v0, v0, v6
	v_lshlrev_b16_e32 v0, 3, v0
	v_lshlrev_b32_e32 v10, 1, v0
	v_mad_u32_u24 v0, v1, s0, v10
	ds_read_b128 v[6:9], v0
	v_add_u32_e32 v0, s28, v1
	v_mad_i64_i32 v[0:1], s[0:1], v0, s6, v[12:13]
	v_lshl_add_u64 v[0:1], v[0:1], 0, v[10:11]
	s_waitcnt lgkmcnt(1)
	global_store_dwordx4 v[14:15], v[2:5], off
	s_waitcnt lgkmcnt(0)
	global_store_dwordx4 v[0:1], v[6:9], off
	s_branch .Lpadfill_c0_end
	s_nop 0
	s_nop 0
	s_nop 0
	s_nop 0
	s_nop 0
